# baseline (speedup 1.0000x reference)
_Z12carry_kernelPKDv2_DF16_PDF16_:
	s_load_dwordx4 s[4:7], s[0:1], 0x0
	s_lshl_b32 s1, s2, 1
	s_mul_hi_u32 s3, s2, 0xaaaaaaab
	s_lshr_b32 s0, s2, 3
	s_and_b32 s1, s1, 12
	s_lshr_b32 s3, s3, 4
	s_add_i32 s1, s1, s3
	s_mul_hi_u32 s3, s0, 0x55555556
	s_mul_i32 s3, s3, 3
	s_sub_i32 s0, s0, s3
	s_mul_i32 s1, s1, 6
	s_lshl_b32 s0, s0, 1
	s_add_i32 s1, s1, s0
	s_and_b32 s0, s2, 1
	s_or_b32 s8, s1, s0
	s_mul_hi_u32 s0, s1, 0xaaaaaaab
	s_lshr_b32 s0, s0, 2
	s_bitcmp0_b32 s0, 1
	s_mov_b32 s9, 0
	s_cselect_b64 vcc, -1, 0
	s_lshl_b64 s[0:1], s[8:9], 17
	v_and_b32_e32 v1, 31, v0
	s_waitcnt lgkmcnt(0)
	s_add_u32 s0, s4, s0
	s_addc_u32 s1, s5, s1
	v_lshlrev_b32_e32 v2, 2, v1
	v_mov_b32_e32 v3, 0
	v_and_b32_e32 v56, 0x3e0, v0
	v_sub_u32_e32 v7, 0x3ff, v56
	v_cndmask_b32_e32 v7, v7, v56, vcc
	v_lshl_add_u32 v70, v7, 7, v2
	v_lshlrev_b32_e32 v90, 1, v1
	v_lshl_add_u32 v90, v7, 6, v90
	s_mov_b64 s[10:11], vcc
	s_cmp_lg_u64 s[10:11], 0
	s_cbranch_scc0 .Lca_rev_ld
	global_load_dword v69, v70, s[0:1]
	global_load_dword v68, v70, s[0:1] offset:128
	global_load_dword v67, v70, s[0:1] offset:256
	global_load_dword v66, v70, s[0:1] offset:384
	global_load_dword v65, v70, s[0:1] offset:512
	global_load_dword v64, v70, s[0:1] offset:640
	global_load_dword v63, v70, s[0:1] offset:768
	global_load_dword v62, v70, s[0:1] offset:896
	global_load_dword v61, v70, s[0:1] offset:1024
	global_load_dword v60, v70, s[0:1] offset:1152
	global_load_dword v59, v70, s[0:1] offset:1280
	global_load_dword v58, v70, s[0:1] offset:1408
	global_load_dword v25, v70, s[0:1] offset:1536
	global_load_dword v24, v70, s[0:1] offset:1664
	global_load_dword v23, v70, s[0:1] offset:1792
	global_load_dword v22, v70, s[0:1] offset:1920
	global_load_dword v21, v70, s[0:1] offset:2048
	global_load_dword v20, v70, s[0:1] offset:2176
	global_load_dword v19, v70, s[0:1] offset:2304
	global_load_dword v18, v70, s[0:1] offset:2432
	global_load_dword v17, v70, s[0:1] offset:2560
	global_load_dword v16, v70, s[0:1] offset:2688
	global_load_dword v15, v70, s[0:1] offset:2816
	global_load_dword v14, v70, s[0:1] offset:2944
	global_load_dword v13, v70, s[0:1] offset:3072
	global_load_dword v12, v70, s[0:1] offset:3200
	global_load_dword v11, v70, s[0:1] offset:3328
	global_load_dword v10, v70, s[0:1] offset:3456
	global_load_dword v9, v70, s[0:1] offset:3584
	global_load_dword v8, v70, s[0:1] offset:3712
	global_load_dword v6, v70, s[0:1] offset:3840
	global_load_dword v4, v70, s[0:1] offset:3968
	s_branch .Lca_ld_done
.Lca_rev_ld:
	global_load_dword v69, v70, s[0:1]
	global_load_dword v68, v70, s[0:1] offset:-128
	global_load_dword v67, v70, s[0:1] offset:-256
	global_load_dword v66, v70, s[0:1] offset:-384
	global_load_dword v65, v70, s[0:1] offset:-512
	global_load_dword v64, v70, s[0:1] offset:-640
	global_load_dword v63, v70, s[0:1] offset:-768
	global_load_dword v62, v70, s[0:1] offset:-896
	global_load_dword v61, v70, s[0:1] offset:-1024
	global_load_dword v60, v70, s[0:1] offset:-1152
	global_load_dword v59, v70, s[0:1] offset:-1280
	global_load_dword v58, v70, s[0:1] offset:-1408
	global_load_dword v25, v70, s[0:1] offset:-1536
	global_load_dword v24, v70, s[0:1] offset:-1664
	global_load_dword v23, v70, s[0:1] offset:-1792
	global_load_dword v22, v70, s[0:1] offset:-1920
	global_load_dword v21, v70, s[0:1] offset:-2048
	global_load_dword v20, v70, s[0:1] offset:-2176
	global_load_dword v19, v70, s[0:1] offset:-2304
	global_load_dword v18, v70, s[0:1] offset:-2432
	global_load_dword v17, v70, s[0:1] offset:-2560
	global_load_dword v16, v70, s[0:1] offset:-2688
	global_load_dword v15, v70, s[0:1] offset:-2816
	global_load_dword v14, v70, s[0:1] offset:-2944
	global_load_dword v13, v70, s[0:1] offset:-3072
	global_load_dword v12, v70, s[0:1] offset:-3200
	global_load_dword v11, v70, s[0:1] offset:-3328
	global_load_dword v10, v70, s[0:1] offset:-3456
	global_load_dword v9, v70, s[0:1] offset:-3584
	global_load_dword v8, v70, s[0:1] offset:-3712
	global_load_dword v6, v70, s[0:1] offset:-3840
	global_load_dword v4, v70, s[0:1] offset:-3968
.Lca_ld_done:
	s_waitcnt vmcnt(31)
	s_waitcnt vmcnt(30)
	v_fma_mix_f32 v5, v69, v68, 0 op_sel_hi:[1,1,0]
	s_waitcnt vmcnt(29)
	v_fma_mix_f32 v5, v5, v67, 0 op_sel_hi:[0,1,0]
	v_lshrrev_b32_e32 v0, 5, v0
	s_movk_i32 s0, 0x84
	v_mad_u32_u24 v2, v0, s0, v2
	v_lshlrev_b32_e32 v0, 2, v0
	s_waitcnt vmcnt(28)
	v_fma_mix_f32 v5, v5, v66, 0 op_sel_hi:[0,1,0]
	s_waitcnt vmcnt(27)
	v_fma_mix_f32 v5, v5, v65, 0 op_sel_hi:[0,1,0]
	s_waitcnt vmcnt(26)
	v_fma_mix_f32 v5, v5, v64, 0 op_sel_hi:[0,1,0]
	s_waitcnt vmcnt(25)
	v_fma_mix_f32 v5, v5, v63, 0 op_sel_hi:[0,1,0]
	v_mad_u32_u24 v0, v1, s0, v0
	s_waitcnt vmcnt(24)
	v_fma_mix_f32 v5, v5, v62, 0 op_sel_hi:[0,1,0]
	s_waitcnt vmcnt(23)
	v_fma_mix_f32 v5, v5, v61, 0 op_sel_hi:[0,1,0]
	s_waitcnt vmcnt(22)
	v_fma_mix_f32 v5, v5, v60, 0 op_sel_hi:[0,1,0]
	s_waitcnt vmcnt(21)
	v_fma_mix_f32 v5, v5, v59, 0 op_sel_hi:[0,1,0]
	s_waitcnt vmcnt(20)
	v_fma_mix_f32 v5, v5, v58, 0 op_sel_hi:[0,1,0]
	s_waitcnt vmcnt(19)
	v_fma_mix_f32 v5, v5, v25, 0 op_sel_hi:[0,1,0]
	s_waitcnt vmcnt(18)
	v_fma_mix_f32 v5, v5, v24, 0 op_sel_hi:[0,1,0]
	s_waitcnt vmcnt(17)
	v_fma_mix_f32 v5, v5, v23, 0 op_sel_hi:[0,1,0]
	s_waitcnt vmcnt(16)
	v_fma_mix_f32 v5, v5, v22, 0 op_sel_hi:[0,1,0]
	s_waitcnt vmcnt(15)
	v_fma_mix_f32 v5, v5, v21, 0 op_sel_hi:[0,1,0]
	s_waitcnt vmcnt(14)
	v_fma_mix_f32 v5, v5, v20, 0 op_sel_hi:[0,1,0]
	s_waitcnt vmcnt(13)
	v_fma_mix_f32 v5, v5, v19, 0 op_sel_hi:[0,1,0]
	s_waitcnt vmcnt(12)
	v_fma_mix_f32 v5, v5, v18, 0 op_sel_hi:[0,1,0]
	s_waitcnt vmcnt(11)
	v_fma_mix_f32 v5, v5, v17, 0 op_sel_hi:[0,1,0]
	s_waitcnt vmcnt(10)
	v_fma_mix_f32 v5, v5, v16, 0 op_sel_hi:[0,1,0]
	s_waitcnt vmcnt(9)
	v_fma_mix_f32 v5, v5, v15, 0 op_sel_hi:[0,1,0]
	s_waitcnt vmcnt(8)
	v_fma_mix_f32 v5, v5, v14, 0 op_sel_hi:[0,1,0]
	s_waitcnt vmcnt(7)
	v_fma_mix_f32 v5, v5, v13, 0 op_sel_hi:[0,1,0]
	s_waitcnt vmcnt(6)
	v_fma_mix_f32 v5, v5, v12, 0 op_sel_hi:[0,1,0]
	s_waitcnt vmcnt(5)
	v_fma_mix_f32 v5, v5, v11, 0 op_sel_hi:[0,1,0]
	s_waitcnt vmcnt(4)
	v_fma_mix_f32 v5, v5, v10, 0 op_sel_hi:[0,1,0]
	v_fma_mix_f32 v57, v69, 0, v69 op_sel:[0,0,1] op_sel_hi:[1,0,1]
	s_waitcnt vmcnt(3)
	v_fma_mix_f32 v5, v5, v9, 0 op_sel_hi:[0,1,0]
	v_fma_mix_f32 v57, v57, v68, v68 op_sel:[0,0,1] op_sel_hi:[0,1,1]
	v_fma_mix_f32 v57, v57, v67, v67 op_sel:[0,0,1] op_sel_hi:[0,1,1]
	v_fma_mix_f32 v57, v57, v66, v66 op_sel:[0,0,1] op_sel_hi:[0,1,1]
	v_fma_mix_f32 v57, v57, v65, v65 op_sel:[0,0,1] op_sel_hi:[0,1,1]
	v_fma_mix_f32 v57, v57, v64, v64 op_sel:[0,0,1] op_sel_hi:[0,1,1]
	v_fma_mix_f32 v57, v57, v63, v63 op_sel:[0,0,1] op_sel_hi:[0,1,1]
	v_fma_mix_f32 v57, v57, v62, v62 op_sel:[0,0,1] op_sel_hi:[0,1,1]
	v_fma_mix_f32 v57, v57, v61, v61 op_sel:[0,0,1] op_sel_hi:[0,1,1]
	v_fma_mix_f32 v57, v57, v60, v60 op_sel:[0,0,1] op_sel_hi:[0,1,1]
	v_fma_mix_f32 v57, v57, v59, v59 op_sel:[0,0,1] op_sel_hi:[0,1,1]
	v_fma_mix_f32 v57, v57, v58, v58 op_sel:[0,0,1] op_sel_hi:[0,1,1]
	v_fma_mix_f32 v57, v57, v25, v25 op_sel:[0,0,1] op_sel_hi:[0,1,1]
	v_fma_mix_f32 v57, v57, v24, v24 op_sel:[0,0,1] op_sel_hi:[0,1,1]
	v_fma_mix_f32 v57, v57, v23, v23 op_sel:[0,0,1] op_sel_hi:[0,1,1]
	v_fma_mix_f32 v57, v57, v22, v22 op_sel:[0,0,1] op_sel_hi:[0,1,1]
	v_fma_mix_f32 v57, v57, v21, v21 op_sel:[0,0,1] op_sel_hi:[0,1,1]
	v_fma_mix_f32 v57, v57, v20, v20 op_sel:[0,0,1] op_sel_hi:[0,1,1]
	v_fma_mix_f32 v57, v57, v19, v19 op_sel:[0,0,1] op_sel_hi:[0,1,1]
	v_fma_mix_f32 v57, v57, v18, v18 op_sel:[0,0,1] op_sel_hi:[0,1,1]
	v_fma_mix_f32 v57, v57, v17, v17 op_sel:[0,0,1] op_sel_hi:[0,1,1]
	v_fma_mix_f32 v57, v57, v16, v16 op_sel:[0,0,1] op_sel_hi:[0,1,1]
	v_fma_mix_f32 v57, v57, v15, v15 op_sel:[0,0,1] op_sel_hi:[0,1,1]
	v_fma_mix_f32 v57, v57, v14, v14 op_sel:[0,0,1] op_sel_hi:[0,1,1]
	v_fma_mix_f32 v57, v57, v13, v13 op_sel:[0,0,1] op_sel_hi:[0,1,1]
	s_waitcnt vmcnt(2)
	v_fma_mix_f32 v5, v5, v8, 0 op_sel_hi:[0,1,0]
	v_fma_mix_f32 v57, v57, v12, v12 op_sel:[0,0,1] op_sel_hi:[0,1,1]
	s_waitcnt vmcnt(1)
	v_fma_mix_f32 v5, v5, v6, 0 op_sel_hi:[0,1,0]
	v_fma_mix_f32 v57, v57, v11, v11 op_sel:[0,0,1] op_sel_hi:[0,1,1]
	v_fma_mix_f32 v57, v57, v10, v10 op_sel:[0,0,1] op_sel_hi:[0,1,1]
	s_waitcnt vmcnt(0)
	v_fma_mix_f32 v5, v5, v4, 0 op_sel_hi:[0,1,0]
	v_fma_mix_f32 v57, v57, v9, v9 op_sel:[0,0,1] op_sel_hi:[0,1,1]
	v_fma_mix_f32 v57, v57, v8, v8 op_sel:[0,0,1] op_sel_hi:[0,1,1]
	v_fma_mix_f32 v57, v57, v6, v6 op_sel:[0,0,1] op_sel_hi:[0,1,1]
	v_fma_mix_f32 v4, v57, v4, v4 op_sel:[0,0,1] op_sel_hi:[0,1,1]
	ds_write_b32 v2, v5 offset:8448
	ds_write_b32 v2, v4 offset:4224
	v_mbcnt_lo_u32_b32 v4, -1, 0
	s_waitcnt lgkmcnt(0)
	s_barrier
	v_mbcnt_hi_u32_b32 v4, -1, v4
	ds_read_b32 v70, v0 offset:4224
	ds_read_b32 v71, v0 offset:8448
	v_and_b32_e32 v5, 0x60, v4
	v_add_u32_e32 v57, -1, v4
	v_cmp_lt_i32_e32 vcc, v57, v5
	v_add_u32_e32 v73, -2, v4
	v_cmp_lt_i32_e64 s[0:1], v73, v5
	v_cndmask_b32_e32 v57, v57, v4, vcc
	v_lshlrev_b32_e32 v57, 2, v57
	s_waitcnt lgkmcnt(1)
	ds_bpermute_b32 v72, v57, v70
	v_cmp_eq_u32_e32 vcc, 0, v1
	v_cndmask_b32_e64 v73, v73, v4, s[0:1]
	v_lshlrev_b32_e32 v73, 2, v73
	v_cmp_gt_u32_e64 s[0:1], 2, v1
	s_waitcnt lgkmcnt(0)
	v_fma_f32 v72, v71, v72, v70
	v_cndmask_b32_e32 v70, v72, v70, vcc
	ds_bpermute_b32 v72, v57, v71
	ds_bpermute_b32 v74, v73, v70
	s_waitcnt lgkmcnt(1)
	v_mul_f32_e32 v72, v71, v72
	v_cndmask_b32_e32 v71, v72, v71, vcc
	s_waitcnt lgkmcnt(0)
	v_fma_f32 v72, v71, v74, v70
	v_cndmask_b32_e64 v70, v72, v70, s[0:1]
	ds_bpermute_b32 v72, v73, v71
	v_add_u32_e32 v73, -4, v4
	v_cmp_lt_i32_e64 s[2:3], v73, v5
	s_waitcnt lgkmcnt(0)
	v_mul_f32_e32 v72, v71, v72
	v_cndmask_b32_e64 v73, v73, v4, s[2:3]
	v_lshlrev_b32_e32 v73, 2, v73
	ds_bpermute_b32 v74, v73, v70
	v_cndmask_b32_e64 v71, v72, v71, s[0:1]
	v_cmp_gt_u32_e64 s[0:1], 4, v1
	s_waitcnt lgkmcnt(0)
	v_fma_f32 v72, v71, v74, v70
	v_cndmask_b32_e64 v70, v72, v70, s[0:1]
	ds_bpermute_b32 v72, v73, v71
	v_add_u32_e32 v73, -8, v4
	v_cmp_lt_i32_e64 s[2:3], v73, v5
	s_waitcnt lgkmcnt(0)
	v_mul_f32_e32 v72, v71, v72
	v_cndmask_b32_e64 v73, v73, v4, s[2:3]
	v_lshlrev_b32_e32 v73, 2, v73
	ds_bpermute_b32 v74, v73, v70
	v_cndmask_b32_e64 v71, v72, v71, s[0:1]
	v_cmp_gt_u32_e64 s[0:1], 8, v1
	s_waitcnt lgkmcnt(0)
	v_fma_f32 v72, v71, v74, v70
	v_cndmask_b32_e64 v70, v72, v70, s[0:1]
	ds_bpermute_b32 v72, v73, v71
	v_add_u32_e32 v73, -16, v4
	v_cmp_lt_i32_e64 s[2:3], v73, v5
	s_waitcnt lgkmcnt(0)
	v_mul_f32_e32 v5, v71, v72
	v_cndmask_b32_e64 v4, v73, v4, s[2:3]
	v_lshlrev_b32_e32 v4, 2, v4
	ds_bpermute_b32 v4, v4, v70
	v_cndmask_b32_e64 v5, v5, v71, s[0:1]
	v_cmp_gt_u32_e64 s[0:1], 16, v1
	s_waitcnt lgkmcnt(0)
	v_fma_f32 v4, v5, v4, v70
	v_cndmask_b32_e64 v4, v4, v70, s[0:1]
	ds_bpermute_b32 v4, v57, v4
	s_lshl_b64 s[0:1], s[8:9], 16
	s_add_u32 s0, s6, s0
	s_addc_u32 s1, s7, s1
	s_waitcnt lgkmcnt(0)
	v_cndmask_b32_e64 v4, v4, 0, vcc
	ds_write_b32 v0, v4
	s_waitcnt lgkmcnt(0)
	s_barrier
	s_cmp_lg_u64 s[10:11], 0
	s_cbranch_scc0 .Lca_rev_st
	ds_read_b32 v57, v2
	s_waitcnt lgkmcnt(0)
	v_cvt_f16_f32_e32 v70, v57
	v_fma_mixlo_f16 v26, v57, v69, v69 op_sel:[0,0,1] op_sel_hi:[0,1,1]
	global_store_short v90, v70, s[0:1]
	global_store_short v90, v26, s[0:1] offset:64
	v_fma_mix_f32 v26, v57, v69, v69 op_sel:[0,0,1] op_sel_hi:[0,1,1]
	v_fma_mixlo_f16 v27, v26, v68, v68 op_sel:[0,0,1] op_sel_hi:[0,1,1]
	v_fma_mix_f32 v26, v26, v68, v68 op_sel:[0,0,1] op_sel_hi:[0,1,1]
	global_store_short v90, v27, s[0:1] offset:128
	v_fma_mixlo_f16 v27, v26, v67, v67 op_sel:[0,0,1] op_sel_hi:[0,1,1]
	v_fma_mix_f32 v26, v26, v67, v67 op_sel:[0,0,1] op_sel_hi:[0,1,1]
	global_store_short v90, v27, s[0:1] offset:192
	v_fma_mixlo_f16 v27, v26, v66, v66 op_sel:[0,0,1] op_sel_hi:[0,1,1]
	v_fma_mix_f32 v2, v26, v66, v66 op_sel:[0,0,1] op_sel_hi:[0,1,1]
	global_store_short v90, v27, s[0:1] offset:256
	v_fma_mix_f32 v26, v2, v65, v65 op_sel:[0,0,1] op_sel_hi:[0,1,1]
	v_fma_mixlo_f16 v27, v2, v65, v65 op_sel:[0,0,1] op_sel_hi:[0,1,1]
	global_store_short v90, v27, s[0:1] offset:320
	v_fma_mix_f32 v27, v26, v64, v64 op_sel:[0,0,1] op_sel_hi:[0,1,1]
	v_fma_mixlo_f16 v26, v26, v64, v64 op_sel:[0,0,1] op_sel_hi:[0,1,1]
	global_store_short v90, v26, s[0:1] offset:384
	v_fma_mix_f32 v26, v27, v63, v63 op_sel:[0,0,1] op_sel_hi:[0,1,1]
	v_fma_mixlo_f16 v27, v27, v63, v63 op_sel:[0,0,1] op_sel_hi:[0,1,1]
	global_store_short v90, v27, s[0:1] offset:448
	v_fma_mix_f32 v27, v26, v62, v62 op_sel:[0,0,1] op_sel_hi:[0,1,1]
	v_fma_mixlo_f16 v26, v26, v62, v62 op_sel:[0,0,1] op_sel_hi:[0,1,1]
	global_store_short v90, v26, s[0:1] offset:512
	v_fma_mix_f32 v26, v27, v61, v61 op_sel:[0,0,1] op_sel_hi:[0,1,1]
	v_fma_mixlo_f16 v27, v27, v61, v61 op_sel:[0,0,1] op_sel_hi:[0,1,1]
	global_store_short v90, v27, s[0:1] offset:576
	v_fma_mix_f32 v27, v26, v60, v60 op_sel:[0,0,1] op_sel_hi:[0,1,1]
	v_fma_mixlo_f16 v26, v26, v60, v60 op_sel:[0,0,1] op_sel_hi:[0,1,1]
	global_store_short v90, v26, s[0:1] offset:640
	v_fma_mix_f32 v26, v27, v59, v59 op_sel:[0,0,1] op_sel_hi:[0,1,1]
	v_fma_mixlo_f16 v27, v27, v59, v59 op_sel:[0,0,1] op_sel_hi:[0,1,1]
	global_store_short v90, v27, s[0:1] offset:704
	v_fma_mix_f32 v27, v26, v58, v58 op_sel:[0,0,1] op_sel_hi:[0,1,1]
	v_fma_mixlo_f16 v26, v26, v58, v58 op_sel:[0,0,1] op_sel_hi:[0,1,1]
	global_store_short v90, v26, s[0:1] offset:768
	v_fma_mix_f32 v26, v27, v25, v25 op_sel:[0,0,1] op_sel_hi:[0,1,1]
	v_fma_mixlo_f16 v25, v27, v25, v25 op_sel:[0,0,1] op_sel_hi:[0,1,1]
	global_store_short v90, v25, s[0:1] offset:832
	v_fma_mix_f32 v25, v26, v24, v24 op_sel:[0,0,1] op_sel_hi:[0,1,1]
	v_fma_mixlo_f16 v24, v26, v24, v24 op_sel:[0,0,1] op_sel_hi:[0,1,1]
	global_store_short v90, v24, s[0:1] offset:896
	v_fma_mix_f32 v24, v25, v23, v23 op_sel:[0,0,1] op_sel_hi:[0,1,1]
	v_fma_mixlo_f16 v23, v25, v23, v23 op_sel:[0,0,1] op_sel_hi:[0,1,1]
	global_store_short v90, v23, s[0:1] offset:960
	v_fma_mix_f32 v23, v24, v22, v22 op_sel:[0,0,1] op_sel_hi:[0,1,1]
	v_fma_mixlo_f16 v22, v24, v22, v22 op_sel:[0,0,1] op_sel_hi:[0,1,1]
	global_store_short v90, v22, s[0:1] offset:1024
	v_fma_mix_f32 v22, v23, v21, v21 op_sel:[0,0,1] op_sel_hi:[0,1,1]
	v_fma_mixlo_f16 v21, v23, v21, v21 op_sel:[0,0,1] op_sel_hi:[0,1,1]
	global_store_short v90, v21, s[0:1] offset:1088
	v_fma_mix_f32 v21, v22, v20, v20 op_sel:[0,0,1] op_sel_hi:[0,1,1]
	v_fma_mixlo_f16 v20, v22, v20, v20 op_sel:[0,0,1] op_sel_hi:[0,1,1]
	global_store_short v90, v20, s[0:1] offset:1152
	v_fma_mix_f32 v20, v21, v19, v19 op_sel:[0,0,1] op_sel_hi:[0,1,1]
	v_fma_mixlo_f16 v19, v21, v19, v19 op_sel:[0,0,1] op_sel_hi:[0,1,1]
	global_store_short v90, v19, s[0:1] offset:1216
	v_fma_mix_f32 v19, v20, v18, v18 op_sel:[0,0,1] op_sel_hi:[0,1,1]
	v_fma_mixlo_f16 v18, v20, v18, v18 op_sel:[0,0,1] op_sel_hi:[0,1,1]
	global_store_short v90, v18, s[0:1] offset:1280
	v_fma_mix_f32 v18, v19, v17, v17 op_sel:[0,0,1] op_sel_hi:[0,1,1]
	v_fma_mixlo_f16 v17, v19, v17, v17 op_sel:[0,0,1] op_sel_hi:[0,1,1]
	global_store_short v90, v17, s[0:1] offset:1344
	v_fma_mix_f32 v17, v18, v16, v16 op_sel:[0,0,1] op_sel_hi:[0,1,1]
	v_fma_mixlo_f16 v16, v18, v16, v16 op_sel:[0,0,1] op_sel_hi:[0,1,1]
	global_store_short v90, v16, s[0:1] offset:1408
	v_fma_mix_f32 v16, v17, v15, v15 op_sel:[0,0,1] op_sel_hi:[0,1,1]
	v_fma_mixlo_f16 v15, v17, v15, v15 op_sel:[0,0,1] op_sel_hi:[0,1,1]
	global_store_short v90, v15, s[0:1] offset:1472
	v_fma_mix_f32 v15, v16, v14, v14 op_sel:[0,0,1] op_sel_hi:[0,1,1]
	v_fma_mixlo_f16 v14, v16, v14, v14 op_sel:[0,0,1] op_sel_hi:[0,1,1]
	global_store_short v90, v14, s[0:1] offset:1536
	v_fma_mix_f32 v14, v15, v13, v13 op_sel:[0,0,1] op_sel_hi:[0,1,1]
	v_fma_mixlo_f16 v13, v15, v13, v13 op_sel:[0,0,1] op_sel_hi:[0,1,1]
	global_store_short v90, v13, s[0:1] offset:1600
	v_fma_mix_f32 v13, v14, v12, v12 op_sel:[0,0,1] op_sel_hi:[0,1,1]
	v_fma_mixlo_f16 v12, v14, v12, v12 op_sel:[0,0,1] op_sel_hi:[0,1,1]
	global_store_short v90, v12, s[0:1] offset:1664
	v_fma_mix_f32 v12, v13, v11, v11 op_sel:[0,0,1] op_sel_hi:[0,1,1]
	v_fma_mixlo_f16 v11, v13, v11, v11 op_sel:[0,0,1] op_sel_hi:[0,1,1]
	global_store_short v90, v11, s[0:1] offset:1728
	v_fma_mix_f32 v11, v12, v10, v10 op_sel:[0,0,1] op_sel_hi:[0,1,1]
	v_fma_mixlo_f16 v10, v12, v10, v10 op_sel:[0,0,1] op_sel_hi:[0,1,1]
	global_store_short v90, v10, s[0:1] offset:1792
	v_fma_mix_f32 v10, v11, v9, v9 op_sel:[0,0,1] op_sel_hi:[0,1,1]
	v_fma_mixlo_f16 v9, v11, v9, v9 op_sel:[0,0,1] op_sel_hi:[0,1,1]
	global_store_short v90, v9, s[0:1] offset:1856
	v_fma_mix_f32 v9, v10, v8, v8 op_sel:[0,0,1] op_sel_hi:[0,1,1]
	v_fma_mixlo_f16 v8, v10, v8, v8 op_sel:[0,0,1] op_sel_hi:[0,1,1]
	global_store_short v90, v8, s[0:1] offset:1920
	v_fma_mixlo_f16 v4, v9, v6, v6 op_sel:[0,0,1] op_sel_hi:[0,1,1]
	global_store_short v90, v4, s[0:1] offset:1984
	s_endpgm
.Lca_rev_st:
	ds_read_b32 v57, v2
	s_waitcnt lgkmcnt(0)
	v_cvt_f16_f32_e32 v70, v57
	v_fma_mixlo_f16 v26, v57, v69, v69 op_sel:[0,0,1] op_sel_hi:[0,1,1]
	global_store_short v90, v70, s[0:1]
	global_store_short v90, v26, s[0:1] offset:-64
	v_fma_mix_f32 v26, v57, v69, v69 op_sel:[0,0,1] op_sel_hi:[0,1,1]
	v_fma_mixlo_f16 v27, v26, v68, v68 op_sel:[0,0,1] op_sel_hi:[0,1,1]
	v_fma_mix_f32 v26, v26, v68, v68 op_sel:[0,0,1] op_sel_hi:[0,1,1]
	global_store_short v90, v27, s[0:1] offset:-128
	v_fma_mixlo_f16 v27, v26, v67, v67 op_sel:[0,0,1] op_sel_hi:[0,1,1]
	v_fma_mix_f32 v26, v26, v67, v67 op_sel:[0,0,1] op_sel_hi:[0,1,1]
	global_store_short v90, v27, s[0:1] offset:-192
	v_fma_mixlo_f16 v27, v26, v66, v66 op_sel:[0,0,1] op_sel_hi:[0,1,1]
	v_fma_mix_f32 v2, v26, v66, v66 op_sel:[0,0,1] op_sel_hi:[0,1,1]
	global_store_short v90, v27, s[0:1] offset:-256
	v_fma_mix_f32 v26, v2, v65, v65 op_sel:[0,0,1] op_sel_hi:[0,1,1]
	v_fma_mixlo_f16 v27, v2, v65, v65 op_sel:[0,0,1] op_sel_hi:[0,1,1]
	global_store_short v90, v27, s[0:1] offset:-320
	v_fma_mix_f32 v27, v26, v64, v64 op_sel:[0,0,1] op_sel_hi:[0,1,1]
	v_fma_mixlo_f16 v26, v26, v64, v64 op_sel:[0,0,1] op_sel_hi:[0,1,1]
	global_store_short v90, v26, s[0:1] offset:-384
	v_fma_mix_f32 v26, v27, v63, v63 op_sel:[0,0,1] op_sel_hi:[0,1,1]
	v_fma_mixlo_f16 v27, v27, v63, v63 op_sel:[0,0,1] op_sel_hi:[0,1,1]
	global_store_short v90, v27, s[0:1] offset:-448
	v_fma_mix_f32 v27, v26, v62, v62 op_sel:[0,0,1] op_sel_hi:[0,1,1]
	v_fma_mixlo_f16 v26, v26, v62, v62 op_sel:[0,0,1] op_sel_hi:[0,1,1]
	global_store_short v90, v26, s[0:1] offset:-512
	v_fma_mix_f32 v26, v27, v61, v61 op_sel:[0,0,1] op_sel_hi:[0,1,1]
	v_fma_mixlo_f16 v27, v27, v61, v61 op_sel:[0,0,1] op_sel_hi:[0,1,1]
	global_store_short v90, v27, s[0:1] offset:-576
	v_fma_mix_f32 v27, v26, v60, v60 op_sel:[0,0,1] op_sel_hi:[0,1,1]
	v_fma_mixlo_f16 v26, v26, v60, v60 op_sel:[0,0,1] op_sel_hi:[0,1,1]
	global_store_short v90, v26, s[0:1] offset:-640
	v_fma_mix_f32 v26, v27, v59, v59 op_sel:[0,0,1] op_sel_hi:[0,1,1]
	v_fma_mixlo_f16 v27, v27, v59, v59 op_sel:[0,0,1] op_sel_hi:[0,1,1]
	global_store_short v90, v27, s[0:1] offset:-704
	v_fma_mix_f32 v27, v26, v58, v58 op_sel:[0,0,1] op_sel_hi:[0,1,1]
	v_fma_mixlo_f16 v26, v26, v58, v58 op_sel:[0,0,1] op_sel_hi:[0,1,1]
	global_store_short v90, v26, s[0:1] offset:-768
	v_fma_mix_f32 v26, v27, v25, v25 op_sel:[0,0,1] op_sel_hi:[0,1,1]
	v_fma_mixlo_f16 v25, v27, v25, v25 op_sel:[0,0,1] op_sel_hi:[0,1,1]
	global_store_short v90, v25, s[0:1] offset:-832
	v_fma_mix_f32 v25, v26, v24, v24 op_sel:[0,0,1] op_sel_hi:[0,1,1]
	v_fma_mixlo_f16 v24, v26, v24, v24 op_sel:[0,0,1] op_sel_hi:[0,1,1]
	global_store_short v90, v24, s[0:1] offset:-896
	v_fma_mix_f32 v24, v25, v23, v23 op_sel:[0,0,1] op_sel_hi:[0,1,1]
	v_fma_mixlo_f16 v23, v25, v23, v23 op_sel:[0,0,1] op_sel_hi:[0,1,1]
	global_store_short v90, v23, s[0:1] offset:-960
	v_fma_mix_f32 v23, v24, v22, v22 op_sel:[0,0,1] op_sel_hi:[0,1,1]
	v_fma_mixlo_f16 v22, v24, v22, v22 op_sel:[0,0,1] op_sel_hi:[0,1,1]
	global_store_short v90, v22, s[0:1] offset:-1024
	v_fma_mix_f32 v22, v23, v21, v21 op_sel:[0,0,1] op_sel_hi:[0,1,1]
	v_fma_mixlo_f16 v21, v23, v21, v21 op_sel:[0,0,1] op_sel_hi:[0,1,1]
	global_store_short v90, v21, s[0:1] offset:-1088
	v_fma_mix_f32 v21, v22, v20, v20 op_sel:[0,0,1] op_sel_hi:[0,1,1]
	v_fma_mixlo_f16 v20, v22, v20, v20 op_sel:[0,0,1] op_sel_hi:[0,1,1]
	global_store_short v90, v20, s[0:1] offset:-1152
	v_fma_mix_f32 v20, v21, v19, v19 op_sel:[0,0,1] op_sel_hi:[0,1,1]
	v_fma_mixlo_f16 v19, v21, v19, v19 op_sel:[0,0,1] op_sel_hi:[0,1,1]
	global_store_short v90, v19, s[0:1] offset:-1216
	v_fma_mix_f32 v19, v20, v18, v18 op_sel:[0,0,1] op_sel_hi:[0,1,1]
	v_fma_mixlo_f16 v18, v20, v18, v18 op_sel:[0,0,1] op_sel_hi:[0,1,1]
	global_store_short v90, v18, s[0:1] offset:-1280
	v_fma_mix_f32 v18, v19, v17, v17 op_sel:[0,0,1] op_sel_hi:[0,1,1]
	v_fma_mixlo_f16 v17, v19, v17, v17 op_sel:[0,0,1] op_sel_hi:[0,1,1]
	global_store_short v90, v17, s[0:1] offset:-1344
	v_fma_mix_f32 v17, v18, v16, v16 op_sel:[0,0,1] op_sel_hi:[0,1,1]
	v_fma_mixlo_f16 v16, v18, v16, v16 op_sel:[0,0,1] op_sel_hi:[0,1,1]
	global_store_short v90, v16, s[0:1] offset:-1408
	v_fma_mix_f32 v16, v17, v15, v15 op_sel:[0,0,1] op_sel_hi:[0,1,1]
	v_fma_mixlo_f16 v15, v17, v15, v15 op_sel:[0,0,1] op_sel_hi:[0,1,1]
	global_store_short v90, v15, s[0:1] offset:-1472
	v_fma_mix_f32 v15, v16, v14, v14 op_sel:[0,0,1] op_sel_hi:[0,1,1]
	v_fma_mixlo_f16 v14, v16, v14, v14 op_sel:[0,0,1] op_sel_hi:[0,1,1]
	global_store_short v90, v14, s[0:1] offset:-1536
	v_fma_mix_f32 v14, v15, v13, v13 op_sel:[0,0,1] op_sel_hi:[0,1,1]
	v_fma_mixlo_f16 v13, v15, v13, v13 op_sel:[0,0,1] op_sel_hi:[0,1,1]
	global_store_short v90, v13, s[0:1] offset:-1600
	v_fma_mix_f32 v13, v14, v12, v12 op_sel:[0,0,1] op_sel_hi:[0,1,1]
	v_fma_mixlo_f16 v12, v14, v12, v12 op_sel:[0,0,1] op_sel_hi:[0,1,1]
	global_store_short v90, v12, s[0:1] offset:-1664
	v_fma_mix_f32 v12, v13, v11, v11 op_sel:[0,0,1] op_sel_hi:[0,1,1]
	v_fma_mixlo_f16 v11, v13, v11, v11 op_sel:[0,0,1] op_sel_hi:[0,1,1]
	global_store_short v90, v11, s[0:1] offset:-1728
	v_fma_mix_f32 v11, v12, v10, v10 op_sel:[0,0,1] op_sel_hi:[0,1,1]
	v_fma_mixlo_f16 v10, v12, v10, v10 op_sel:[0,0,1] op_sel_hi:[0,1,1]
	global_store_short v90, v10, s[0:1] offset:-1792
	v_fma_mix_f32 v10, v11, v9, v9 op_sel:[0,0,1] op_sel_hi:[0,1,1]
	v_fma_mixlo_f16 v9, v11, v9, v9 op_sel:[0,0,1] op_sel_hi:[0,1,1]
	global_store_short v90, v9, s[0:1] offset:-1856
	v_fma_mix_f32 v9, v10, v8, v8 op_sel:[0,0,1] op_sel_hi:[0,1,1]
	v_fma_mixlo_f16 v8, v10, v8, v8 op_sel:[0,0,1] op_sel_hi:[0,1,1]
	global_store_short v90, v8, s[0:1] offset:-1920
	v_fma_mixlo_f16 v4, v9, v6, v6 op_sel:[0,0,1] op_sel_hi:[0,1,1]
	global_store_short v90, v4, s[0:1] offset:-1984
	s_endpgm

	.amdhsa_kernel _Z12carry_kernelPKDv2_DF16_PDF16_
		.amdhsa_group_segment_fixed_size 12672
		.amdhsa_private_segment_fixed_size 0
		.amdhsa_kernarg_size 16
		.amdhsa_user_sgpr_count 2
		.amdhsa_user_sgpr_dispatch_ptr 0
		.amdhsa_user_sgpr_queue_ptr 0
		.amdhsa_user_sgpr_kernarg_segment_ptr 1
		.amdhsa_user_sgpr_dispatch_id 0
		.amdhsa_user_sgpr_kernarg_preload_length 0
		.amdhsa_user_sgpr_kernarg_preload_offset 0
		.amdhsa_user_sgpr_private_segment_size 0
		.amdhsa_uses_dynamic_stack 0
		.amdhsa_enable_private_segment 0
		.amdhsa_system_sgpr_workgroup_id_x 1
		.amdhsa_system_sgpr_workgroup_id_y 0
		.amdhsa_system_sgpr_workgroup_id_z 0
		.amdhsa_system_sgpr_workgroup_info 0
		.amdhsa_system_vgpr_workitem_id 0
		.amdhsa_next_free_vgpr 92
		.amdhsa_next_free_sgpr 12
		.amdhsa_accum_offset 92
		.amdhsa_reserve_vcc 1
		.amdhsa_float_round_mode_32 0
		.amdhsa_float_round_mode_16_64 0
		.amdhsa_float_denorm_mode_32 3
		.amdhsa_float_denorm_mode_16_64 3
		.amdhsa_dx10_clamp 1
		.amdhsa_ieee_mode 1
		.amdhsa_fp16_overflow 0
		.amdhsa_tg_split 0
		.amdhsa_exception_fp_ieee_invalid_op 0
		.amdhsa_exception_fp_denorm_src 0
		.amdhsa_exception_fp_ieee_div_zero 0
		.amdhsa_exception_fp_ieee_overflow 0
		.amdhsa_exception_fp_ieee_underflow 0
		.amdhsa_exception_fp_ieee_inexact 0
		.amdhsa_exception_int_div_zero 0
	.end_amdhsa_kernel

amdhsa.kernels:
  - .agpr_count:     0
    .args:
      - .actual_access:  read_only
        .address_space:  global
        .offset:         0
        .size:           8
        .value_kind:     global_buffer
      - .actual_access:  read_only
        .address_space:  global
        .offset:         8
        .size:           8
        .value_kind:     global_buffer
      - .actual_access:  read_only
        .address_space:  global
        .offset:         16
        .size:           8
        .value_kind:     global_buffer
      - .actual_access:  read_only
        .address_space:  global
        .offset:         24
        .size:           8
        .value_kind:     global_buffer
      - .actual_access:  read_only
        .address_space:  global
        .offset:         32
        .size:           8
        .value_kind:     global_buffer
      - .actual_access:  read_only
        .address_space:  global
        .offset:         40
        .size:           8
        .value_kind:     global_buffer
      - .actual_access:  write_only
        .address_space:  global
        .offset:         48
        .size:           8
        .value_kind:     global_buffer
      - .actual_access:  write_only
        .address_space:  global
        .offset:         56
        .size:           8
        .value_kind:     global_buffer
      - .actual_access:  write_only
        .address_space:  global
        .offset:         64
        .size:           8
        .value_kind:     global_buffer
      - .actual_access:  write_only
        .address_space:  global
        .offset:         72
        .size:           8
        .value_kind:     global_buffer
    .group_segment_fixed_size: 65536
    .kernarg_segment_align: 8
    .kernarg_segment_size: 80
    .language:       OpenCL C
    .language_version:
      - 2
      - 0
    .max_flat_workgroup_size: 256
    .name:           _Z11proj_kernelPKfS0_S0_S0_S0_S0_PDF16_S1_PfS2_
    .private_segment_fixed_size: 0
    .sgpr_count:     22
    .sgpr_spill_count: 0
    .symbol:         _Z11proj_kernelPKfS0_S0_S0_S0_S0_PDF16_S1_PfS2_.kd
    .uniform_work_group_size: 1
    .uses_dynamic_stack: false
    .vgpr_count:     200
    .vgpr_spill_count: 0
    .wavefront_size: 64
  - .agpr_count:     0
    .args:
      - .actual_access:  read_only
        .address_space:  global
        .offset:         0
        .size:           8
        .value_kind:     global_buffer
      - .actual_access:  write_only
        .address_space:  global
        .offset:         8
        .size:           8
        .value_kind:     global_buffer
    .group_segment_fixed_size: 12672
    .kernarg_segment_align: 8
    .kernarg_segment_size: 16
    .language:       OpenCL C
    .language_version:
      - 2
      - 0
    .max_flat_workgroup_size: 1024
    .name:           _Z12carry_kernelPKDv2_DF16_PDF16_
    .private_segment_fixed_size: 0
    .sgpr_count:     18
    .sgpr_spill_count: 0
    .symbol:         _Z12carry_kernelPKDv2_DF16_PDF16_.kd
    .uniform_work_group_size: 1
    .uses_dynamic_stack: false
    .vgpr_count:     92
    .vgpr_spill_count: 0
    .wavefront_size: 64
  - .agpr_count:     0
    .args:
      - .actual_access:  read_only
        .address_space:  global
        .offset:         0
        .size:           8
        .value_kind:     global_buffer
      - .actual_access:  read_only
        .address_space:  global
        .offset:         8
        .size:           8
        .value_kind:     global_buffer
      - .actual_access:  read_only
        .address_space:  global
        .offset:         16
        .size:           8
        .value_kind:     global_buffer
      - .actual_access:  read_only
        .address_space:  global
        .offset:         24
        .size:           8
        .value_kind:     global_buffer
      - .actual_access:  read_only
        .address_space:  global
        .offset:         32
        .size:           8
        .value_kind:     global_buffer
      - .actual_access:  write_only
        .address_space:  global
        .offset:         40
        .size:           8
        .value_kind:     global_buffer
      - .actual_access:  read_only
        .address_space:  global
        .offset:         48
        .size:           8
        .value_kind:     global_buffer
      - .actual_access:  read_only
        .address_space:  global
        .offset:         56
        .size:           8
        .value_kind:     global_buffer
    .group_segment_fixed_size: 33280
    .kernarg_segment_align: 8
    .kernarg_segment_size: 64
    .language:       OpenCL C
    .language_version:
      - 2
      - 0
    .max_flat_workgroup_size: 256
    .name:           _Z11scan_kernelILi1ELi1536ELi4EEvPKfPKDF16_S3_S1_S1_PDv2_DF16_S3_Pf
    .private_segment_fixed_size: 0
    .sgpr_count:     24
    .sgpr_spill_count: 0
    .symbol:         _Z11scan_kernelILi1ELi1536ELi4EEvPKfPKDF16_S3_S1_S1_PDv2_DF16_S3_Pf.kd
    .uniform_work_group_size: 1
    .uses_dynamic_stack: false
    .vgpr_count:     110
    .vgpr_spill_count: 0
    .wavefront_size: 64
  - .agpr_count:     0
    .args:
      - .actual_access:  read_only
        .address_space:  global
        .offset:         0
        .size:           8
        .value_kind:     global_buffer
      - .actual_access:  read_only
        .address_space:  global
        .offset:         8
        .size:           8
        .value_kind:     global_buffer
      - .actual_access:  read_only
        .address_space:  global
        .offset:         16
        .size:           8
        .value_kind:     global_buffer
      - .actual_access:  read_only
        .address_space:  global
        .offset:         24
        .size:           8
        .value_kind:     global_buffer
      - .actual_access:  read_only
        .address_space:  global
        .offset:         32
        .size:           8
        .value_kind:     global_buffer
      - .actual_access:  read_only
        .address_space:  global
        .offset:         40
        .size:           8
        .value_kind:     global_buffer
      - .actual_access:  read_only
        .address_space:  global
        .offset:         48
        .size:           8
        .value_kind:     global_buffer
      - .actual_access:  write_only
        .address_space:  global
        .offset:         56
        .size:           8
        .value_kind:     global_buffer
    .group_segment_fixed_size: 50176
    .kernarg_segment_align: 8
    .kernarg_segment_size: 64
    .language:       OpenCL C
    .language_version:
      - 2
      - 0
    .max_flat_workgroup_size: 256
    .name:           _Z11scan_kernelILi3ELi1536ELi3EEvPKfPKDF16_S3_S1_S1_PDv2_DF16_S3_Pf
    .private_segment_fixed_size: 0
    .sgpr_count:     28
    .sgpr_spill_count: 0
    .symbol:         _Z11scan_kernelILi3ELi1536ELi3EEvPKfPKDF16_S3_S1_S1_PDv2_DF16_S3_Pf.kd
    .uniform_work_group_size: 1
    .uses_dynamic_stack: false
    .vgpr_count:     168
    .vgpr_spill_count: 0
    .wavefront_size: 64
